# t21
# speedup vs baseline: 1.0415x; 1.0415x over previous
.Ljoin:
	s_barrier
	v_mov_b32_e32 v6, 0x6000
	ds_read_b96 v[32:34], v6
	ds_read_b96 v[36:38], v6 offset:16
	ds_read_b96 v[40:42], v6 offset:32
	ds_read_b96 v[44:46], v6 offset:48
	v_add_u32_e32 v56, 0xc00, v3
	v_add_u32_e32 v57, 0x1200, v3
	ds_read2_b32 v[8:9], v3 offset0:0 offset1:1
	ds_read_b32 v24, v3 offset:8
	ds_read2_b32 v[10:11], v3 offset0:192 offset1:193
	ds_read_b32 v25, v3 offset:776
	ds_read2_b32 v[12:13], v4 offset0:0 offset1:1
	ds_read_b32 v26, v4 offset:8
	s_waitcnt lgkmcnt(4)
	v_fma_f32 v60, v8, v32, v44
	v_fma_f32 v61, v8, v33, v45
	v_fma_f32 v62, v8, v34, v46
	v_fmac_f32_e32 v60, v9, v36
	v_fmac_f32_e32 v61, v9, v37
	v_fmac_f32_e32 v62, v9, v38
	v_fmac_f32_e32 v60, v24, v40
	v_fmac_f32_e32 v61, v24, v41
	v_fmac_f32_e32 v62, v24, v42
	ds_write2_b32 v3, v60, v61 offset0:0 offset1:1
	ds_write_b32 v3, v62 offset:8
	ds_read2_b32 v[14:15], v4 offset0:192 offset1:193
	ds_read_b32 v27, v4 offset:776
	s_waitcnt lgkmcnt(6)
	v_fma_f32 v35, v10, v32, v44
	v_fma_f32 v39, v10, v33, v45
	v_fma_f32 v43, v10, v34, v46
	v_fmac_f32_e32 v35, v11, v36
	v_fmac_f32_e32 v39, v11, v37
	v_fmac_f32_e32 v43, v11, v38
	v_fmac_f32_e32 v35, v25, v40
	v_fmac_f32_e32 v39, v25, v41
	v_fmac_f32_e32 v43, v25, v42
	ds_write2_b32 v3, v35, v39 offset0:192 offset1:193
	ds_write_b32 v3, v43 offset:776
	ds_read2_b32 v[16:17], v56 offset0:0 offset1:1
	ds_read_b32 v28, v56 offset:8
	s_waitcnt lgkmcnt(8)
	v_fma_f32 v60, v12, v32, v44
	v_fma_f32 v61, v12, v33, v45
	v_fma_f32 v62, v12, v34, v46
	v_fmac_f32_e32 v60, v13, v36
	v_fmac_f32_e32 v61, v13, v37
	v_fmac_f32_e32 v62, v13, v38
	v_fmac_f32_e32 v60, v26, v40
	v_fmac_f32_e32 v61, v26, v41
	v_fmac_f32_e32 v62, v26, v42
	ds_write2_b32 v4, v60, v61 offset0:0 offset1:1
	ds_write_b32 v4, v62 offset:8
	ds_read2_b32 v[18:19], v56 offset0:192 offset1:193
	ds_read_b32 v29, v56 offset:776
	s_waitcnt lgkmcnt(8)
	v_fma_f32 v35, v14, v32, v44
	v_fma_f32 v39, v14, v33, v45
	v_fma_f32 v43, v14, v34, v46
	v_fmac_f32_e32 v35, v15, v36
	v_fmac_f32_e32 v39, v15, v37
	v_fmac_f32_e32 v43, v15, v38
	v_fmac_f32_e32 v35, v27, v40
	v_fmac_f32_e32 v39, v27, v41
	v_fmac_f32_e32 v43, v27, v42
	ds_write2_b32 v4, v35, v39 offset0:192 offset1:193
	ds_write_b32 v4, v43 offset:776
	ds_read2_b32 v[20:21], v57 offset0:0 offset1:1
	ds_read_b32 v30, v57 offset:8
	s_waitcnt lgkmcnt(8)
	v_fma_f32 v60, v16, v32, v44
	v_fma_f32 v61, v16, v33, v45
	v_fma_f32 v62, v16, v34, v46
	v_fmac_f32_e32 v60, v17, v36
	v_fmac_f32_e32 v61, v17, v37
	v_fmac_f32_e32 v62, v17, v38
	v_fmac_f32_e32 v60, v28, v40
	v_fmac_f32_e32 v61, v28, v41
	v_fmac_f32_e32 v62, v28, v42
	ds_write2_b32 v56, v60, v61 offset0:0 offset1:1
	ds_write_b32 v56, v62 offset:8
	ds_read2_b32 v[22:23], v57 offset0:192 offset1:193
	ds_read_b32 v31, v57 offset:776
	s_waitcnt lgkmcnt(8)
	v_fma_f32 v35, v18, v32, v44
	v_fma_f32 v39, v18, v33, v45
	v_fma_f32 v43, v18, v34, v46
	v_fmac_f32_e32 v35, v19, v36
	v_fmac_f32_e32 v39, v19, v37
	v_fmac_f32_e32 v43, v19, v38
	v_fmac_f32_e32 v35, v29, v40
	v_fmac_f32_e32 v39, v29, v41
	v_fmac_f32_e32 v43, v29, v42
	ds_write2_b32 v56, v35, v39 offset0:192 offset1:193
	ds_write_b32 v56, v43 offset:776
	s_waitcnt lgkmcnt(6)
	v_fma_f32 v60, v20, v32, v44
	v_fma_f32 v61, v20, v33, v45
	v_fma_f32 v62, v20, v34, v46
	v_fmac_f32_e32 v60, v21, v36
	v_fmac_f32_e32 v61, v21, v37
	v_fmac_f32_e32 v62, v21, v38
	v_fmac_f32_e32 v60, v30, v40
	v_fmac_f32_e32 v61, v30, v41
	v_fmac_f32_e32 v62, v30, v42
	ds_write2_b32 v57, v60, v61 offset0:0 offset1:1
	ds_write_b32 v57, v62 offset:8
	s_waitcnt lgkmcnt(4)
	v_fma_f32 v35, v22, v32, v44
	v_fma_f32 v39, v22, v33, v45
	v_fma_f32 v43, v22, v34, v46
	v_fmac_f32_e32 v35, v23, v36
	v_fmac_f32_e32 v39, v23, v37
	v_fmac_f32_e32 v43, v23, v38
	v_fmac_f32_e32 v35, v31, v40
	v_fmac_f32_e32 v39, v31, v41
	v_fmac_f32_e32 v43, v31, v42
	ds_write2_b32 v57, v35, v39 offset0:192 offset1:193
	ds_write_b32 v57, v43 offset:776
	s_waitcnt lgkmcnt(0)
	s_barrier
	ds_read_b128 v[8:11], v2
	ds_read_b128 v[12:15], v2 offset:1024
	ds_read_b128 v[16:19], v2 offset:2048
	ds_read_b128 v[20:23], v2 offset:3072
	ds_read_b128 v[24:27], v2 offset:4096
	ds_read_b128 v[28:31], v2 offset:5120
	s_waitcnt lgkmcnt(5)
	global_store_dwordx4 v1, v[8:11], s[10:11] offset:-2048 sc1 nt
	s_waitcnt lgkmcnt(4)
	global_store_dwordx4 v1, v[12:15], s[10:11] offset:-1024 sc1 nt
	s_waitcnt lgkmcnt(3)
	global_store_dwordx4 v1, v[16:19], s[10:11] offset:0 sc1 nt
	s_waitcnt lgkmcnt(2)
	global_store_dwordx4 v1, v[20:23], s[10:11] offset:1024 sc1 nt
	s_waitcnt lgkmcnt(1)
	global_store_dwordx4 v1, v[24:27], s[10:11] offset:2048 sc1 nt
	s_waitcnt lgkmcnt(0)
	s_and_saveexec_b64 s[16:17], s[14:15]
	global_store_dwordx4 v1, v[28:31], s[10:11] offset:3072 sc1 nt
	s_endpgm
